# speedup vs baseline: 1.0674x; 1.0674x over previous
_Z11prep_kernelPKfS0_PKiPDF16_S3_PfS4_:
	s_lshl_b32 s14, s2, 2
	v_lshrrev_b32_e32 v1, 8, v0
	v_or_b32_e32 v5, s14, v1
	s_movk_i32 s2, 0xff
	v_and_b32_e32 v4, 0xff, v0
	v_cmp_lt_i32_e32 vcc, s2, v5
	s_and_saveexec_b64 s[2:3], vcc
	s_xor_b64 s[2:3], exec, s[2:3]
	s_cbranch_execz .LBB0_5
	v_readfirstlane_b32 s15, v0
	s_and_b32 s17, s15, 0xff
	s_cmpk_ge_u32 s17, 0xc0
	s_cbranch_scc1 .LBB0_7
	s_and_b32 s16, s17, 0xc0
	s_cmpk_lg_u32 s16, 0x80
	s_cbranch_scc1 .Lprep_full
	s_mov_b32 exec_lo, 0xffffffff
	s_mov_b32 exec_hi, 0x0
.Lprep_full:
	s_load_dwordx4 s[8:11], s[0:1], 0x0
	s_load_dwordx4 s[4:7], s[0:1], 0x18
	v_add_u32_e32 v34, 0xffffff00, v5
	v_mov_b32_e32 v35, 0
	v_lshlrev_b64 v[32:33], 11, v[34:35]
	v_lshl_or_b32 v32, v4, 3, v32
	v_lshlrev_b64 v[0:1], 2, v[32:33]
	s_waitcnt lgkmcnt(0)
	s_cmp_lg_u32 s14, 0x100
	s_cbranch_scc1 .Lprep_noflag
	s_cmp_gt_u32 s15, 63
	s_cbranch_scc1 .Lprep_noflag
	s_add_u32 s16, s4, 0x3c08000
	s_addc_u32 s17, s5, 0
	v_lshlrev_b32_e32 v6, 2, v4
	v_mov_b32_e32 v7, 0
	v_mov_b32_e32 v8, s8
	v_mov_b32_e32 v9, s9
	v_mov_b32_e32 v10, s10
	v_mov_b32_e32 v11, s11
	global_store_dword v6, v7, s[16:17]
	global_store_dword v6, v7, s[16:17] offset:256
	global_store_dword v6, v7, s[16:17] offset:512
	global_store_dwordx4 v7, v[8:11], s[16:17] offset:2048

.LBB1_9:
	s_cmp_lt_i32 s56, 14
	s_cbranch_scc1 .Lqkv_nopoll
	s_cmp_gt_i32 s56, 24
	s_cbranch_scc1 .Lqkv_nopoll
	s_bitcmp1_b32 s56, 1
	s_cbranch_scc0 .Lqkv_chk
	s_sub_u32 s82, s56, 14
	s_lshl_b32 s82, s82, 6
	v_add_u32_e32 v242, s82, v241
	global_load_dword v240, v242, s[80:81] sc1
	s_branch .Lqkv_nopoll

.LBB1_30:
	s_and_b64 vcc, exec, s[4:5]
	s_cbranch_vccz .LBB1_41
	s_load_dwordx4 s[44:47], s[0:1], 0x0
	s_load_dwordx2 s[48:49], s[0:1], 0x20
	s_add_i32 s50, s2, 0xffffff40
	v_and_b32_e32 v1, 31, v0
	v_lshrrev_b32_e32 v2, 5, v0
	v_lshlrev_b32_e32 v3, 5, v1
	v_lshl_add_u32 v3, v2, 13, v3
	v_add_u32_e32 v3, 0x1400, v3
	v_lshlrev_b32_e32 v4, 4, v1
	v_lshl_add_u32 v4, v2, 12, v4
	v_add_u32_e32 v4, 0xa00, v4
	s_waitcnt lgkmcnt(0)
	s_add_u32 s48, s48, 0x408000
	s_addc_u32 s49, s49, 0
	s_load_dwordx4 s[52:55], s[48:49], 0x800
	s_lshl_b32 s51, s50, 18
	s_add_u32 s44, s44, s51
	s_addc_u32 s45, s45, 0
	s_mul_i32 s51, s50, 0x30000
	s_add_u32 s46, s46, s51
	s_addc_u32 s47, s47, 0
	s_waitcnt lgkmcnt(0)
	s_lshl_b32 s51, s50, 19
	s_add_u32 s52, s52, s51
	s_addc_u32 s53, s53, 0
	s_mul_i32 s51, s50, 0x60000
	s_add_u32 s54, s54, s51
	s_addc_u32 s55, s55, 0
	v_cmp_eq_u32_e64 s[78:79], 0, v0
	v_mov_b32_e32 v5, 1
	v_mov_b32_e32 v6, s50
	v_lshlrev_b32_e32 v6, 2, v6
	s_add_u32 s58, s52, 0x0
	s_addc_u32 s59, s53, 0
	global_load_dwordx4 v[16:19], v3, s[58:59] nt
	global_load_dwordx4 v[20:23], v3, s[58:59] offset:16 nt
	s_add_u32 s58, s52, 0x20000
	s_addc_u32 s59, s53, 0
	global_load_dwordx4 v[24:27], v3, s[58:59] nt
	global_load_dwordx4 v[28:31], v3, s[58:59] offset:16 nt
	s_add_u32 s58, s52, 0x40000
	s_addc_u32 s59, s53, 0
	global_load_dwordx4 v[32:35], v3, s[58:59] nt
	global_load_dwordx4 v[36:39], v3, s[58:59] offset:16 nt
	s_add_u32 s58, s52, 0x60000
	s_addc_u32 s59, s53, 0
	global_load_dwordx4 v[40:43], v3, s[58:59] nt
	global_load_dwordx4 v[44:47], v3, s[58:59] offset:16 nt
	s_add_u32 s58, s54, 0x0
	s_addc_u32 s59, s55, 0
	global_load_dwordx4 v[48:51], v3, s[58:59] nt
	global_load_dwordx4 v[52:55], v3, s[58:59] offset:16 nt
	s_add_u32 s58, s54, 0x20000
	s_addc_u32 s59, s55, 0
	global_load_dwordx4 v[56:59], v3, s[58:59] nt
	global_load_dwordx4 v[60:63], v3, s[58:59] offset:16 nt
	s_add_u32 s58, s54, 0x40000
	s_addc_u32 s59, s55, 0
	global_load_dwordx4 v[64:67], v3, s[58:59] nt
	global_load_dwordx4 v[68:71], v3, s[58:59] offset:16 nt
	s_add_u32 s58, s52, 0x400
	s_addc_u32 s59, s53, 0
	global_load_dwordx4 v[72:75], v3, s[58:59] nt
	global_load_dwordx4 v[76:79], v3, s[58:59] offset:16 nt
	s_add_u32 s58, s52, 0x20400
	s_addc_u32 s59, s53, 0
	global_load_dwordx4 v[80:83], v3, s[58:59] nt
	global_load_dwordx4 v[84:87], v3, s[58:59] offset:16 nt
	s_add_u32 s58, s52, 0x40400
	s_addc_u32 s59, s53, 0
	global_load_dwordx4 v[88:91], v3, s[58:59] nt
	global_load_dwordx4 v[92:95], v3, s[58:59] offset:16 nt
	s_add_u32 s58, s52, 0x60400
	s_addc_u32 s59, s53, 0
	global_load_dwordx4 v[96:99], v3, s[58:59] nt
	global_load_dwordx4 v[100:103], v3, s[58:59] offset:16 nt
	s_add_u32 s58, s54, 0x400
	s_addc_u32 s59, s55, 0
	global_load_dwordx4 v[104:107], v3, s[58:59] nt
	global_load_dwordx4 v[108:111], v3, s[58:59] offset:16 nt
	s_add_u32 s58, s54, 0x20400
	s_addc_u32 s59, s55, 0
	global_load_dwordx4 v[112:115], v3, s[58:59] nt
	global_load_dwordx4 v[116:119], v3, s[58:59] offset:16 nt
	s_add_u32 s58, s54, 0x40400
	s_addc_u32 s59, s55, 0
	global_load_dwordx4 v[120:123], v3, s[58:59] nt
	global_load_dwordx4 v[124:127], v3, s[58:59] offset:16 nt
	s_waitcnt vmcnt(26)
	v_cvt_pk_f16_f32 v16, v16, v17
	v_cvt_pk_f16_f32 v17, v18, v19
	v_cvt_pk_f16_f32 v18, v20, v21
	v_cvt_pk_f16_f32 v19, v22, v23
	s_add_u32 s76, s44, 0x0
	s_addc_u32 s77, s45, 0
	global_store_dwordx4 v4, v[16:19], s[76:77] sc1
	s_waitcnt vmcnt(25)
	v_cvt_pk_f16_f32 v24, v24, v25
	v_cvt_pk_f16_f32 v25, v26, v27
	v_cvt_pk_f16_f32 v26, v28, v29
	v_cvt_pk_f16_f32 v27, v30, v31
	s_add_u32 s76, s44, 0x10000
	s_addc_u32 s77, s45, 0
	global_store_dwordx4 v4, v[24:27], s[76:77] sc1
	s_waitcnt vmcnt(24)
	v_cvt_pk_f16_f32 v32, v32, v33
	v_cvt_pk_f16_f32 v33, v34, v35
	v_cvt_pk_f16_f32 v34, v36, v37
	v_cvt_pk_f16_f32 v35, v38, v39
	s_add_u32 s76, s44, 0x20000
	s_addc_u32 s77, s45, 0
	global_store_dwordx4 v4, v[32:35], s[76:77] sc1
	s_waitcnt vmcnt(23)
	v_cvt_pk_f16_f32 v40, v40, v41
	v_cvt_pk_f16_f32 v41, v42, v43
	v_cvt_pk_f16_f32 v42, v44, v45
	v_cvt_pk_f16_f32 v43, v46, v47
	s_add_u32 s76, s44, 0x30000
	s_addc_u32 s77, s45, 0
	global_store_dwordx4 v4, v[40:43], s[76:77] sc1
	s_waitcnt vmcnt(22)
	v_cvt_pk_f16_f32 v48, v48, v49
	v_cvt_pk_f16_f32 v49, v50, v51
	v_cvt_pk_f16_f32 v50, v52, v53
	v_cvt_pk_f16_f32 v51, v54, v55
	s_add_u32 s76, s46, 0x0
	s_addc_u32 s77, s47, 0
	global_store_dwordx4 v4, v[48:51], s[76:77] sc1
	s_waitcnt vmcnt(21)
	v_cvt_pk_f16_f32 v56, v56, v57
	v_cvt_pk_f16_f32 v57, v58, v59
	v_cvt_pk_f16_f32 v58, v60, v61
	v_cvt_pk_f16_f32 v59, v62, v63
	s_add_u32 s76, s46, 0x10000
	s_addc_u32 s77, s47, 0
	global_store_dwordx4 v4, v[56:59], s[76:77] sc1
	s_waitcnt vmcnt(20)
	v_cvt_pk_f16_f32 v64, v64, v65
	v_cvt_pk_f16_f32 v65, v66, v67
	v_cvt_pk_f16_f32 v66, v68, v69
	v_cvt_pk_f16_f32 v67, v70, v71
	s_add_u32 s76, s46, 0x20000
	s_addc_u32 s77, s47, 0
	global_store_dwordx4 v4, v[64:67], s[76:77] sc1
	s_add_u32 s58, s52, 0x800
	s_addc_u32 s59, s53, 0
	global_load_dwordx4 v[16:19], v3, s[58:59] nt
	global_load_dwordx4 v[20:23], v3, s[58:59] offset:16 nt
	s_add_u32 s58, s52, 0x20800
	s_addc_u32 s59, s53, 0
	global_load_dwordx4 v[24:27], v3, s[58:59] nt
	global_load_dwordx4 v[28:31], v3, s[58:59] offset:16 nt
	s_add_u32 s58, s52, 0x40800
	s_addc_u32 s59, s53, 0
	global_load_dwordx4 v[32:35], v3, s[58:59] nt
	global_load_dwordx4 v[36:39], v3, s[58:59] offset:16 nt
	s_add_u32 s58, s52, 0x60800
	s_addc_u32 s59, s53, 0
	global_load_dwordx4 v[40:43], v3, s[58:59] nt
	global_load_dwordx4 v[44:47], v3, s[58:59] offset:16 nt
	s_add_u32 s58, s54, 0x800
	s_addc_u32 s59, s55, 0
	global_load_dwordx4 v[48:51], v3, s[58:59] nt
	global_load_dwordx4 v[52:55], v3, s[58:59] offset:16 nt
	s_add_u32 s58, s54, 0x20800
	s_addc_u32 s59, s55, 0
	global_load_dwordx4 v[56:59], v3, s[58:59] nt
	global_load_dwordx4 v[60:63], v3, s[58:59] offset:16 nt
	s_add_u32 s58, s54, 0x40800
	s_addc_u32 s59, s55, 0
	global_load_dwordx4 v[64:67], v3, s[58:59] nt
	global_load_dwordx4 v[68:71], v3, s[58:59] offset:16 nt
	s_waitcnt vmcnt(33)
	v_cvt_pk_f16_f32 v72, v72, v73
	v_cvt_pk_f16_f32 v73, v74, v75
	v_cvt_pk_f16_f32 v74, v76, v77
	v_cvt_pk_f16_f32 v75, v78, v79
	s_add_u32 s76, s44, 0x200
	s_addc_u32 s77, s45, 0
	global_store_dwordx4 v4, v[72:75], s[76:77] sc1
	s_waitcnt vmcnt(32)
	v_cvt_pk_f16_f32 v80, v80, v81
	v_cvt_pk_f16_f32 v81, v82, v83
	v_cvt_pk_f16_f32 v82, v84, v85
	v_cvt_pk_f16_f32 v83, v86, v87
	s_add_u32 s76, s44, 0x10200
	s_addc_u32 s77, s45, 0
	global_store_dwordx4 v4, v[80:83], s[76:77] sc1
	s_waitcnt vmcnt(31)
	v_cvt_pk_f16_f32 v88, v88, v89
	v_cvt_pk_f16_f32 v89, v90, v91
	v_cvt_pk_f16_f32 v90, v92, v93
	v_cvt_pk_f16_f32 v91, v94, v95
	s_add_u32 s76, s44, 0x20200
	s_addc_u32 s77, s45, 0
	global_store_dwordx4 v4, v[88:91], s[76:77] sc1
	s_waitcnt vmcnt(30)
	v_cvt_pk_f16_f32 v96, v96, v97
	v_cvt_pk_f16_f32 v97, v98, v99
	v_cvt_pk_f16_f32 v98, v100, v101
	v_cvt_pk_f16_f32 v99, v102, v103
	s_add_u32 s76, s44, 0x30200
	s_addc_u32 s77, s45, 0
	global_store_dwordx4 v4, v[96:99], s[76:77] sc1
	s_waitcnt vmcnt(29)
	v_cvt_pk_f16_f32 v104, v104, v105
	v_cvt_pk_f16_f32 v105, v106, v107
	v_cvt_pk_f16_f32 v106, v108, v109
	v_cvt_pk_f16_f32 v107, v110, v111
	s_add_u32 s76, s46, 0x200
	s_addc_u32 s77, s47, 0
	global_store_dwordx4 v4, v[104:107], s[76:77] sc1
	s_waitcnt vmcnt(28)
	v_cvt_pk_f16_f32 v112, v112, v113
	v_cvt_pk_f16_f32 v113, v114, v115
	v_cvt_pk_f16_f32 v114, v116, v117
	v_cvt_pk_f16_f32 v115, v118, v119
	s_add_u32 s76, s46, 0x10200
	s_addc_u32 s77, s47, 0
	global_store_dwordx4 v4, v[112:115], s[76:77] sc1
	s_waitcnt vmcnt(27)
	v_cvt_pk_f16_f32 v120, v120, v121
	v_cvt_pk_f16_f32 v121, v122, v123
	v_cvt_pk_f16_f32 v122, v124, v125
	v_cvt_pk_f16_f32 v123, v126, v127
	s_add_u32 s76, s46, 0x20200
	s_addc_u32 s77, s47, 0
	global_store_dwordx4 v4, v[120:123], s[76:77] sc1
	s_waitcnt vmcnt(21)
	s_barrier
	s_mov_b64 s[56:57], exec
	s_and_b64 exec, exec, s[78:79]
	global_store_dword v6, v5, s[48:49] offset:0 sc1
	s_mov_b64 exec, s[56:57]
	s_waitcnt vmcnt(20)
	v_cvt_pk_f16_f32 v16, v16, v17
	v_cvt_pk_f16_f32 v17, v18, v19
	v_cvt_pk_f16_f32 v18, v20, v21
	v_cvt_pk_f16_f32 v19, v22, v23
	s_add_u32 s76, s44, 0x400
	s_addc_u32 s77, s45, 0
	global_store_dwordx4 v4, v[16:19], s[76:77] sc1
	s_waitcnt vmcnt(19)
	v_cvt_pk_f16_f32 v24, v24, v25
	v_cvt_pk_f16_f32 v25, v26, v27
	v_cvt_pk_f16_f32 v26, v28, v29
	v_cvt_pk_f16_f32 v27, v30, v31
	s_add_u32 s76, s44, 0x10400
	s_addc_u32 s77, s45, 0
	global_store_dwordx4 v4, v[24:27], s[76:77] sc1
	s_waitcnt vmcnt(18)
	v_cvt_pk_f16_f32 v32, v32, v33
	v_cvt_pk_f16_f32 v33, v34, v35
	v_cvt_pk_f16_f32 v34, v36, v37
	v_cvt_pk_f16_f32 v35, v38, v39
	s_add_u32 s76, s44, 0x20400
	s_addc_u32 s77, s45, 0
	global_store_dwordx4 v4, v[32:35], s[76:77] sc1
	s_waitcnt vmcnt(17)
	v_cvt_pk_f16_f32 v40, v40, v41
	v_cvt_pk_f16_f32 v41, v42, v43
	v_cvt_pk_f16_f32 v42, v44, v45
	v_cvt_pk_f16_f32 v43, v46, v47
	s_add_u32 s76, s44, 0x30400
	s_addc_u32 s77, s45, 0
	global_store_dwordx4 v4, v[40:43], s[76:77] sc1
	s_waitcnt vmcnt(16)
	v_cvt_pk_f16_f32 v48, v48, v49
	v_cvt_pk_f16_f32 v49, v50, v51
	v_cvt_pk_f16_f32 v50, v52, v53
	v_cvt_pk_f16_f32 v51, v54, v55
	s_add_u32 s76, s46, 0x400
	s_addc_u32 s77, s47, 0
	global_store_dwordx4 v4, v[48:51], s[76:77] sc1
	s_waitcnt vmcnt(15)
	v_cvt_pk_f16_f32 v56, v56, v57
	v_cvt_pk_f16_f32 v57, v58, v59
	v_cvt_pk_f16_f32 v58, v60, v61
	v_cvt_pk_f16_f32 v59, v62, v63
	s_add_u32 s76, s46, 0x10400
	s_addc_u32 s77, s47, 0
	global_store_dwordx4 v4, v[56:59], s[76:77] sc1
	s_waitcnt vmcnt(14)
	v_cvt_pk_f16_f32 v64, v64, v65
	v_cvt_pk_f16_f32 v65, v66, v67
	v_cvt_pk_f16_f32 v66, v68, v69
	v_cvt_pk_f16_f32 v67, v70, v71
	s_add_u32 s76, s46, 0x20400
	s_addc_u32 s77, s47, 0
	global_store_dwordx4 v4, v[64:67], s[76:77] sc1
	s_waitcnt vmcnt(8)
	s_barrier
	s_mov_b64 s[56:57], exec
	s_and_b64 exec, exec, s[78:79]
	global_store_dword v6, v5, s[48:49] offset:256 sc1
	s_mov_b64 exec, s[56:57]
	s_waitcnt vmcnt(1)
	s_barrier
	s_mov_b64 s[56:57], exec
	s_and_b64 exec, exec, s[78:79]
	global_store_dword v6, v5, s[48:49] offset:512 sc1
	s_mov_b64 exec, s[56:57]
	s_add_i32 s24, s2, 0xffffff40
	s_lshl_b32 s20, s24, 4
	s_lshl_b32 s0, s24, 5
	s_ashr_i32 s21, s20, 31
	s_and_b32 s25, s0, 0xffffffc0
	s_lshl_b64 s[20:21], s[20:21], 2
	v_lshrrev_b32_e32 v6, 6, v0
	s_waitcnt lgkmcnt(0)
	s_add_u32 s26, s30, s20
	s_addc_u32 s27, s31, s21
	v_lshl_or_b32 v2, v6, 3, s25
	s_and_b32 s25, s2, 1
	s_lshl_b32 s2, s25, 7
	s_add_u32 s20, s28, s2
	v_and_b32_e32 v7, 63, v0
	s_mov_b32 s3, 0
	s_addc_u32 s21, s29, 0
	s_bfe_u32 s2, s24, 0x1a0001
	v_add_u32_e32 v2, v2, v7
	v_mov_b32_e32 v3, 0
	s_lshl_b64 s[2:3], s[2:3], 19
	v_lshl_add_u32 v1, v6, 2, 0
	v_lshlrev_b64 v[4:5], 8, v[2:3]
	v_lshl_or_b32 v2, v6, 16, s2
	s_lshl_b32 s2, s25, 12
	v_lshlrev_b32_e32 v6, 2, v7
	v_cmp_gt_u32_e64 s[0:1], 8, v7
	v_cmp_eq_u32_e64 s[22:23], 0, v7
	v_cmp_eq_u32_e64 s[6:7], 1, v7
	v_cmp_eq_u32_e64 s[8:9], 2, v7
	v_cmp_eq_u32_e64 s[10:11], 3, v7
	v_cmp_eq_u32_e64 s[12:13], 4, v7
	v_cmp_eq_u32_e64 s[14:15], 5, v7
	v_cmp_eq_u32_e64 s[16:17], 6, v7
	v_cmp_eq_u32_e64 s[18:19], 7, v7
	v_or3_b32 v6, v2, s2, v6
	v_mov_b32_e32 v7, s3
	v_cmp_eq_u32_e64 s[4:5], 0, v0
	v_lshl_add_u64 v[4:5], s[20:21], 0, v[4:5]
	v_lshl_add_u64 v[6:7], s[42:43], 0, v[6:7]
	s_mov_b64 s[28:29], 0
	s_lshr_b32 s58, s24, 1
	s_lshl_b32 s58, s58, 19
	s_add_u32 s60, s42, s58
	s_addc_u32 s61, s43, 0
	s_add_u32 s62, s60, 0x2000
	s_addc_u32 s63, s61, 0
	s_add_u32 s64, s62, 0x2000
	s_addc_u32 s65, s63, 0
	s_add_u32 s66, s64, 0x2000
	s_addc_u32 s67, s65, 0
	s_add_u32 s68, s66, 0x2000
	s_addc_u32 s69, s67, 0
	s_add_u32 s70, s68, 0x2000
	s_addc_u32 s71, s69, 0
	s_add_u32 s72, s70, 0x2000
	s_addc_u32 s73, s71, 0
	s_add_u32 s74, s72, 0x2000
	s_addc_u32 s75, s73, 0
	v_lshrrev_b32_e32 v96, 6, v0
	v_lshlrev_b32_e32 v96, 16, v96
	v_and_b32_e32 v97, 63, v0
	v_lshl_add_u32 v96, v97, 2, v96
	s_and_b32 s59, s24, 1
	s_lshl_b32 s59, s59, 12
	v_add_u32_e32 v96, s59, v96
	s_mov_b32 s76, 0
	s_mov_b32 s77, 0
	global_load_dword v100, v96, s[60:61] offset:0 nt
	global_load_dword v101, v96, s[62:63] offset:0 nt
	global_load_dword v102, v96, s[64:65] offset:0 nt
	global_load_dword v103, v96, s[66:67] offset:0 nt
	global_load_dword v104, v96, s[68:69] offset:0 nt
	global_load_dword v105, v96, s[70:71] offset:0 nt
	global_load_dword v106, v96, s[72:73] offset:0 nt
	global_load_dword v107, v96, s[74:75] offset:0 nt
	global_load_dword v108, v96, s[60:61] offset:256 nt
	global_load_dword v109, v96, s[62:63] offset:256 nt
	global_load_dword v110, v96, s[64:65] offset:256 nt
	global_load_dword v111, v96, s[66:67] offset:256 nt
	global_load_dword v112, v96, s[68:69] offset:256 nt
	global_load_dword v113, v96, s[70:71] offset:256 nt
	global_load_dword v114, v96, s[72:73] offset:256 nt
	global_load_dword v115, v96, s[74:75] offset:256 nt
	global_load_dword v116, v96, s[60:61] offset:512 nt
	global_load_dword v117, v96, s[62:63] offset:512 nt
	global_load_dword v118, v96, s[64:65] offset:512 nt
	global_load_dword v119, v96, s[66:67] offset:512 nt
	global_load_dword v120, v96, s[68:69] offset:512 nt
	global_load_dword v121, v96, s[70:71] offset:512 nt
	global_load_dword v122, v96, s[72:73] offset:512 nt
	global_load_dword v123, v96, s[74:75] offset:512 nt
	global_load_dword v124, v96, s[60:61] offset:768 nt
	global_load_dword v125, v96, s[62:63] offset:768 nt
	global_load_dword v126, v96, s[64:65] offset:768 nt
	global_load_dword v127, v96, s[66:67] offset:768 nt
	global_load_dword v128, v96, s[68:69] offset:768 nt
	global_load_dword v129, v96, s[70:71] offset:768 nt
	global_load_dword v130, v96, s[72:73] offset:768 nt
	global_load_dword v131, v96, s[74:75] offset:768 nt
	global_load_dword v132, v96, s[60:61] offset:1024 nt
	global_load_dword v133, v96, s[62:63] offset:1024 nt
	global_load_dword v134, v96, s[64:65] offset:1024 nt
	global_load_dword v135, v96, s[66:67] offset:1024 nt
	global_load_dword v136, v96, s[68:69] offset:1024 nt
	global_load_dword v137, v96, s[70:71] offset:1024 nt
	global_load_dword v138, v96, s[72:73] offset:1024 nt
	global_load_dword v139, v96, s[74:75] offset:1024 nt
	global_load_dword v140, v96, s[60:61] offset:1280 nt
	global_load_dword v141, v96, s[62:63] offset:1280 nt
	global_load_dword v142, v96, s[64:65] offset:1280 nt
	global_load_dword v143, v96, s[66:67] offset:1280 nt
	global_load_dword v144, v96, s[68:69] offset:1280 nt
	global_load_dword v145, v96, s[70:71] offset:1280 nt
	global_load_dword v146, v96, s[72:73] offset:1280 nt
	global_load_dword v147, v96, s[74:75] offset:1280 nt
	global_load_dword v148, v96, s[60:61] offset:1536 nt
	global_load_dword v149, v96, s[62:63] offset:1536 nt
	global_load_dword v150, v96, s[64:65] offset:1536 nt
	global_load_dword v151, v96, s[66:67] offset:1536 nt
	global_load_dword v152, v96, s[68:69] offset:1536 nt
	global_load_dword v153, v96, s[70:71] offset:1536 nt
	global_load_dword v154, v96, s[72:73] offset:1536 nt
	global_load_dword v155, v96, s[74:75] offset:1536 nt
	s_waitcnt vmcnt(48)
	v_cmp_ne_u32_e32 vcc, 0, v100
	s_nop 1
	v_mov_b32_e32 v2, vcc_lo
	v_mov_b32_e32 v9, vcc_hi
	v_cmp_ne_u32_e32 vcc, 0, v101
	v_cndmask_b32_e64 v2, 0, v2, s[22:23]
	v_cndmask_b32_e64 v9, 0, v9, s[22:23]
	v_mov_b32_e32 v11, vcc_hi
	v_mov_b32_e32 v14, vcc_lo
	v_cndmask_b32_e64 v9, v9, v11, s[6:7]
	v_cndmask_b32_e64 v2, v2, v14, s[6:7]
	v_cmp_ne_u32_e32 vcc, 0, v102
	s_nop 1
	v_mov_b32_e32 v11, vcc_lo
	v_mov_b32_e32 v14, vcc_hi
	v_cmp_ne_u32_e32 vcc, 0, v103
	v_cndmask_b32_e64 v2, v2, v11, s[8:9]
	v_cndmask_b32_e64 v9, v9, v14, s[8:9]
	v_mov_b32_e32 v11, vcc_hi
	v_mov_b32_e32 v14, vcc_lo
	v_cmp_ne_u32_e32 vcc, 0, v104
	v_cndmask_b32_e64 v9, v9, v11, s[10:11]
	v_cndmask_b32_e64 v2, v2, v14, s[10:11]
	v_mov_b32_e32 v11, vcc_lo
	v_mov_b32_e32 v12, vcc_hi
	v_cmp_ne_u32_e32 vcc, 0, v105
	v_cndmask_b32_e64 v2, v2, v11, s[12:13]
	v_cndmask_b32_e64 v9, v9, v12, s[12:13]
	v_mov_b32_e32 v11, vcc_hi
	v_mov_b32_e32 v12, vcc_lo
	v_cndmask_b32_e64 v9, v9, v11, s[14:15]
	v_cndmask_b32_e64 v2, v2, v12, s[14:15]
	v_cmp_ne_u32_e32 vcc, 0, v106
	s_nop 1
	v_mov_b32_e32 v10, vcc_lo
	v_mov_b32_e32 v11, vcc_hi
	v_cmp_ne_u32_e32 vcc, 0, v107
	v_cndmask_b32_e64 v2, v2, v10, s[16:17]
	v_cndmask_b32_e64 v8, v9, v11, s[16:17]
	v_mov_b32_e32 v9, vcc_hi
	v_mov_b32_e32 v10, vcc_lo
	v_cndmask_b32_e64 v9, v8, v9, s[18:19]
	v_cndmask_b32_e64 v8, v2, v10, s[18:19]
	s_mov_b64 s[2:3], exec
	s_mov_b64 exec, s[0:1]
	global_store_dwordx2 v[4:5], v[8:9], off
	s_mov_b64 exec, s[2:3]
	v_cmp_ne_u64_e32 vcc, 0, v[8:9]
	s_and_b64 s[20:21], s[0:1], vcc
	s_cmp_lg_u64 s[20:21], 0
	s_cselect_b32 s20, 1, 0
	s_or_b32 s76, s76, s20
	v_cmp_ne_u64_e32 vcc, -1, v[8:9]
	s_and_b64 s[20:21], s[0:1], vcc
	s_cmp_lg_u64 s[20:21], 0
	s_cselect_b32 s20, 1, 0
	s_or_b32 s77, s77, s20
	v_lshl_add_u64 v[4:5], v[4:5], 0, 8
	global_load_dword v156, v96, s[60:61] offset:1792 nt
	global_load_dword v157, v96, s[62:63] offset:1792 nt
	global_load_dword v158, v96, s[64:65] offset:1792 nt
	global_load_dword v159, v96, s[66:67] offset:1792 nt
	global_load_dword v160, v96, s[68:69] offset:1792 nt
	global_load_dword v161, v96, s[70:71] offset:1792 nt
	global_load_dword v162, v96, s[72:73] offset:1792 nt
	global_load_dword v163, v96, s[74:75] offset:1792 nt
	s_waitcnt vmcnt(49)
	v_cmp_ne_u32_e32 vcc, 0, v108
	s_nop 1
	v_mov_b32_e32 v2, vcc_lo
	v_mov_b32_e32 v9, vcc_hi
	v_cmp_ne_u32_e32 vcc, 0, v109
	v_cndmask_b32_e64 v2, 0, v2, s[22:23]
	v_cndmask_b32_e64 v9, 0, v9, s[22:23]
	v_mov_b32_e32 v11, vcc_hi
	v_mov_b32_e32 v14, vcc_lo
	v_cndmask_b32_e64 v9, v9, v11, s[6:7]
	v_cndmask_b32_e64 v2, v2, v14, s[6:7]
	v_cmp_ne_u32_e32 vcc, 0, v110
	s_nop 1
	v_mov_b32_e32 v11, vcc_lo
	v_mov_b32_e32 v14, vcc_hi
	v_cmp_ne_u32_e32 vcc, 0, v111
	v_cndmask_b32_e64 v2, v2, v11, s[8:9]
	v_cndmask_b32_e64 v9, v9, v14, s[8:9]
	v_mov_b32_e32 v11, vcc_hi
	v_mov_b32_e32 v14, vcc_lo
	v_cmp_ne_u32_e32 vcc, 0, v112
	v_cndmask_b32_e64 v9, v9, v11, s[10:11]
	v_cndmask_b32_e64 v2, v2, v14, s[10:11]
	v_mov_b32_e32 v11, vcc_lo
	v_mov_b32_e32 v12, vcc_hi
	v_cmp_ne_u32_e32 vcc, 0, v113
	v_cndmask_b32_e64 v2, v2, v11, s[12:13]
	v_cndmask_b32_e64 v9, v9, v12, s[12:13]
	v_mov_b32_e32 v11, vcc_hi
	v_mov_b32_e32 v12, vcc_lo
	v_cndmask_b32_e64 v9, v9, v11, s[14:15]
	v_cndmask_b32_e64 v2, v2, v12, s[14:15]
	v_cmp_ne_u32_e32 vcc, 0, v114
	s_nop 1
	v_mov_b32_e32 v10, vcc_lo
	v_mov_b32_e32 v11, vcc_hi
	v_cmp_ne_u32_e32 vcc, 0, v115
	v_cndmask_b32_e64 v2, v2, v10, s[16:17]
	v_cndmask_b32_e64 v8, v9, v11, s[16:17]
	v_mov_b32_e32 v9, vcc_hi
	v_mov_b32_e32 v10, vcc_lo
	v_cndmask_b32_e64 v9, v8, v9, s[18:19]
	v_cndmask_b32_e64 v8, v2, v10, s[18:19]
	s_mov_b64 s[2:3], exec
	s_mov_b64 exec, s[0:1]
	global_store_dwordx2 v[4:5], v[8:9], off
	s_mov_b64 exec, s[2:3]
	v_cmp_ne_u64_e32 vcc, 0, v[8:9]
	s_and_b64 s[20:21], s[0:1], vcc
	s_cmp_lg_u64 s[20:21], 0
	s_cselect_b32 s20, 2, 0
	s_or_b32 s76, s76, s20
	v_cmp_ne_u64_e32 vcc, -1, v[8:9]
	s_and_b64 s[20:21], s[0:1], vcc
	s_cmp_lg_u64 s[20:21], 0
	s_cselect_b32 s20, 2, 0
	s_or_b32 s77, s77, s20
	v_lshl_add_u64 v[4:5], v[4:5], 0, 8
	global_load_dword v164, v96, s[60:61] offset:2048 nt
	global_load_dword v165, v96, s[62:63] offset:2048 nt
	global_load_dword v166, v96, s[64:65] offset:2048 nt
	global_load_dword v167, v96, s[66:67] offset:2048 nt
	global_load_dword v168, v96, s[68:69] offset:2048 nt
	global_load_dword v169, v96, s[70:71] offset:2048 nt
	global_load_dword v170, v96, s[72:73] offset:2048 nt
	global_load_dword v171, v96, s[74:75] offset:2048 nt
	s_waitcnt vmcnt(50)
	v_cmp_ne_u32_e32 vcc, 0, v116
	s_nop 1
	v_mov_b32_e32 v2, vcc_lo
	v_mov_b32_e32 v9, vcc_hi
	v_cmp_ne_u32_e32 vcc, 0, v117
	v_cndmask_b32_e64 v2, 0, v2, s[22:23]
	v_cndmask_b32_e64 v9, 0, v9, s[22:23]
	v_mov_b32_e32 v11, vcc_hi
	v_mov_b32_e32 v14, vcc_lo
	v_cndmask_b32_e64 v9, v9, v11, s[6:7]
	v_cndmask_b32_e64 v2, v2, v14, s[6:7]
	v_cmp_ne_u32_e32 vcc, 0, v118
	s_nop 1
	v_mov_b32_e32 v11, vcc_lo
	v_mov_b32_e32 v14, vcc_hi
	v_cmp_ne_u32_e32 vcc, 0, v119
	v_cndmask_b32_e64 v2, v2, v11, s[8:9]
	v_cndmask_b32_e64 v9, v9, v14, s[8:9]
	v_mov_b32_e32 v11, vcc_hi
	v_mov_b32_e32 v14, vcc_lo
	v_cmp_ne_u32_e32 vcc, 0, v120
	v_cndmask_b32_e64 v9, v9, v11, s[10:11]
	v_cndmask_b32_e64 v2, v2, v14, s[10:11]
	v_mov_b32_e32 v11, vcc_lo
	v_mov_b32_e32 v12, vcc_hi
	v_cmp_ne_u32_e32 vcc, 0, v121
	v_cndmask_b32_e64 v2, v2, v11, s[12:13]
	v_cndmask_b32_e64 v9, v9, v12, s[12:13]
	v_mov_b32_e32 v11, vcc_hi
	v_mov_b32_e32 v12, vcc_lo
	v_cndmask_b32_e64 v9, v9, v11, s[14:15]
	v_cndmask_b32_e64 v2, v2, v12, s[14:15]
	v_cmp_ne_u32_e32 vcc, 0, v122
	s_nop 1
	v_mov_b32_e32 v10, vcc_lo
	v_mov_b32_e32 v11, vcc_hi
	v_cmp_ne_u32_e32 vcc, 0, v123
	v_cndmask_b32_e64 v2, v2, v10, s[16:17]
	v_cndmask_b32_e64 v8, v9, v11, s[16:17]
	v_mov_b32_e32 v9, vcc_hi
	v_mov_b32_e32 v10, vcc_lo
	v_cndmask_b32_e64 v9, v8, v9, s[18:19]
	v_cndmask_b32_e64 v8, v2, v10, s[18:19]
	s_mov_b64 s[2:3], exec
	s_mov_b64 exec, s[0:1]
	global_store_dwordx2 v[4:5], v[8:9], off
	s_mov_b64 exec, s[2:3]
	v_cmp_ne_u64_e32 vcc, 0, v[8:9]
	s_and_b64 s[20:21], s[0:1], vcc
	s_cmp_lg_u64 s[20:21], 0
	s_cselect_b32 s20, 4, 0
	s_or_b32 s76, s76, s20
	v_cmp_ne_u64_e32 vcc, -1, v[8:9]
	s_and_b64 s[20:21], s[0:1], vcc
	s_cmp_lg_u64 s[20:21], 0
	s_cselect_b32 s20, 4, 0
	s_or_b32 s77, s77, s20
	v_lshl_add_u64 v[4:5], v[4:5], 0, 8
	global_load_dword v172, v96, s[60:61] offset:2304 nt
	global_load_dword v173, v96, s[62:63] offset:2304 nt
	global_load_dword v174, v96, s[64:65] offset:2304 nt
	global_load_dword v175, v96, s[66:67] offset:2304 nt
	global_load_dword v176, v96, s[68:69] offset:2304 nt
	global_load_dword v177, v96, s[70:71] offset:2304 nt
	global_load_dword v178, v96, s[72:73] offset:2304 nt
	global_load_dword v179, v96, s[74:75] offset:2304 nt
	s_waitcnt vmcnt(51)
	v_cmp_ne_u32_e32 vcc, 0, v124
	s_nop 1
	v_mov_b32_e32 v2, vcc_lo
	v_mov_b32_e32 v9, vcc_hi
	v_cmp_ne_u32_e32 vcc, 0, v125
	v_cndmask_b32_e64 v2, 0, v2, s[22:23]
	v_cndmask_b32_e64 v9, 0, v9, s[22:23]
	v_mov_b32_e32 v11, vcc_hi
	v_mov_b32_e32 v14, vcc_lo
	v_cndmask_b32_e64 v9, v9, v11, s[6:7]
	v_cndmask_b32_e64 v2, v2, v14, s[6:7]
	v_cmp_ne_u32_e32 vcc, 0, v126
	s_nop 1
	v_mov_b32_e32 v11, vcc_lo
	v_mov_b32_e32 v14, vcc_hi
	v_cmp_ne_u32_e32 vcc, 0, v127
	v_cndmask_b32_e64 v2, v2, v11, s[8:9]
	v_cndmask_b32_e64 v9, v9, v14, s[8:9]
	v_mov_b32_e32 v11, vcc_hi
	v_mov_b32_e32 v14, vcc_lo
	v_cmp_ne_u32_e32 vcc, 0, v128
	v_cndmask_b32_e64 v9, v9, v11, s[10:11]
	v_cndmask_b32_e64 v2, v2, v14, s[10:11]
	v_mov_b32_e32 v11, vcc_lo
	v_mov_b32_e32 v12, vcc_hi
	v_cmp_ne_u32_e32 vcc, 0, v129
	v_cndmask_b32_e64 v2, v2, v11, s[12:13]
	v_cndmask_b32_e64 v9, v9, v12, s[12:13]
	v_mov_b32_e32 v11, vcc_hi
	v_mov_b32_e32 v12, vcc_lo
	v_cndmask_b32_e64 v9, v9, v11, s[14:15]
	v_cndmask_b32_e64 v2, v2, v12, s[14:15]
	v_cmp_ne_u32_e32 vcc, 0, v130
	s_nop 1
	v_mov_b32_e32 v10, vcc_lo
	v_mov_b32_e32 v11, vcc_hi
	v_cmp_ne_u32_e32 vcc, 0, v131
	v_cndmask_b32_e64 v2, v2, v10, s[16:17]
	v_cndmask_b32_e64 v8, v9, v11, s[16:17]
	v_mov_b32_e32 v9, vcc_hi
	v_mov_b32_e32 v10, vcc_lo
	v_cndmask_b32_e64 v9, v8, v9, s[18:19]
	v_cndmask_b32_e64 v8, v2, v10, s[18:19]
	s_mov_b64 s[2:3], exec
	s_mov_b64 exec, s[0:1]
	global_store_dwordx2 v[4:5], v[8:9], off
	s_mov_b64 exec, s[2:3]
	v_cmp_ne_u64_e32 vcc, 0, v[8:9]
	s_and_b64 s[20:21], s[0:1], vcc
	s_cmp_lg_u64 s[20:21], 0
	s_cselect_b32 s20, 8, 0
	s_or_b32 s76, s76, s20
	v_cmp_ne_u64_e32 vcc, -1, v[8:9]
	s_and_b64 s[20:21], s[0:1], vcc
	s_cmp_lg_u64 s[20:21], 0
	s_cselect_b32 s20, 8, 0
	s_or_b32 s77, s77, s20
	v_lshl_add_u64 v[4:5], v[4:5], 0, 8
	global_load_dword v180, v96, s[60:61] offset:2560 nt
	global_load_dword v181, v96, s[62:63] offset:2560 nt
	global_load_dword v182, v96, s[64:65] offset:2560 nt
	global_load_dword v183, v96, s[66:67] offset:2560 nt
	global_load_dword v184, v96, s[68:69] offset:2560 nt
	global_load_dword v185, v96, s[70:71] offset:2560 nt
	global_load_dword v186, v96, s[72:73] offset:2560 nt
	global_load_dword v187, v96, s[74:75] offset:2560 nt
	s_waitcnt vmcnt(52)
	v_cmp_ne_u32_e32 vcc, 0, v132
	s_nop 1
	v_mov_b32_e32 v2, vcc_lo
	v_mov_b32_e32 v9, vcc_hi
	v_cmp_ne_u32_e32 vcc, 0, v133
	v_cndmask_b32_e64 v2, 0, v2, s[22:23]
	v_cndmask_b32_e64 v9, 0, v9, s[22:23]
	v_mov_b32_e32 v11, vcc_hi
	v_mov_b32_e32 v14, vcc_lo
	v_cndmask_b32_e64 v9, v9, v11, s[6:7]
	v_cndmask_b32_e64 v2, v2, v14, s[6:7]
	v_cmp_ne_u32_e32 vcc, 0, v134
	s_nop 1
	v_mov_b32_e32 v11, vcc_lo
	v_mov_b32_e32 v14, vcc_hi
	v_cmp_ne_u32_e32 vcc, 0, v135
	v_cndmask_b32_e64 v2, v2, v11, s[8:9]
	v_cndmask_b32_e64 v9, v9, v14, s[8:9]
	v_mov_b32_e32 v11, vcc_hi
	v_mov_b32_e32 v14, vcc_lo
	v_cmp_ne_u32_e32 vcc, 0, v136
	v_cndmask_b32_e64 v9, v9, v11, s[10:11]
	v_cndmask_b32_e64 v2, v2, v14, s[10:11]
	v_mov_b32_e32 v11, vcc_lo
	v_mov_b32_e32 v12, vcc_hi
	v_cmp_ne_u32_e32 vcc, 0, v137
	v_cndmask_b32_e64 v2, v2, v11, s[12:13]
	v_cndmask_b32_e64 v9, v9, v12, s[12:13]
	v_mov_b32_e32 v11, vcc_hi
	v_mov_b32_e32 v12, vcc_lo
	v_cndmask_b32_e64 v9, v9, v11, s[14:15]
	v_cndmask_b32_e64 v2, v2, v12, s[14:15]
	v_cmp_ne_u32_e32 vcc, 0, v138
	s_nop 1
	v_mov_b32_e32 v10, vcc_lo
	v_mov_b32_e32 v11, vcc_hi
	v_cmp_ne_u32_e32 vcc, 0, v139
	v_cndmask_b32_e64 v2, v2, v10, s[16:17]
	v_cndmask_b32_e64 v8, v9, v11, s[16:17]
	v_mov_b32_e32 v9, vcc_hi
	v_mov_b32_e32 v10, vcc_lo
	v_cndmask_b32_e64 v9, v8, v9, s[18:19]
	v_cndmask_b32_e64 v8, v2, v10, s[18:19]
	s_mov_b64 s[2:3], exec
	s_mov_b64 exec, s[0:1]
	global_store_dwordx2 v[4:5], v[8:9], off
	s_mov_b64 exec, s[2:3]
	v_cmp_ne_u64_e32 vcc, 0, v[8:9]
	s_and_b64 s[20:21], s[0:1], vcc
	s_cmp_lg_u64 s[20:21], 0
	s_cselect_b32 s20, 16, 0
	s_or_b32 s76, s76, s20
	v_cmp_ne_u64_e32 vcc, -1, v[8:9]
	s_and_b64 s[20:21], s[0:1], vcc
	s_cmp_lg_u64 s[20:21], 0
	s_cselect_b32 s20, 16, 0
	s_or_b32 s77, s77, s20
	v_lshl_add_u64 v[4:5], v[4:5], 0, 8
	global_load_dword v188, v96, s[60:61] offset:2816 nt
	global_load_dword v189, v96, s[62:63] offset:2816 nt
	global_load_dword v190, v96, s[64:65] offset:2816 nt
	global_load_dword v191, v96, s[66:67] offset:2816 nt
	global_load_dword v192, v96, s[68:69] offset:2816 nt
	global_load_dword v193, v96, s[70:71] offset:2816 nt
	global_load_dword v194, v96, s[72:73] offset:2816 nt
	global_load_dword v195, v96, s[74:75] offset:2816 nt
	s_waitcnt vmcnt(53)
	v_cmp_ne_u32_e32 vcc, 0, v140
	s_nop 1
	v_mov_b32_e32 v2, vcc_lo
	v_mov_b32_e32 v9, vcc_hi
	v_cmp_ne_u32_e32 vcc, 0, v141
	v_cndmask_b32_e64 v2, 0, v2, s[22:23]
	v_cndmask_b32_e64 v9, 0, v9, s[22:23]
	v_mov_b32_e32 v11, vcc_hi
	v_mov_b32_e32 v14, vcc_lo
	v_cndmask_b32_e64 v9, v9, v11, s[6:7]
	v_cndmask_b32_e64 v2, v2, v14, s[6:7]
	v_cmp_ne_u32_e32 vcc, 0, v142
	s_nop 1
	v_mov_b32_e32 v11, vcc_lo
	v_mov_b32_e32 v14, vcc_hi
	v_cmp_ne_u32_e32 vcc, 0, v143
	v_cndmask_b32_e64 v2, v2, v11, s[8:9]
	v_cndmask_b32_e64 v9, v9, v14, s[8:9]
	v_mov_b32_e32 v11, vcc_hi
	v_mov_b32_e32 v14, vcc_lo
	v_cmp_ne_u32_e32 vcc, 0, v144
	v_cndmask_b32_e64 v9, v9, v11, s[10:11]
	v_cndmask_b32_e64 v2, v2, v14, s[10:11]
	v_mov_b32_e32 v11, vcc_lo
	v_mov_b32_e32 v12, vcc_hi
	v_cmp_ne_u32_e32 vcc, 0, v145
	v_cndmask_b32_e64 v2, v2, v11, s[12:13]
	v_cndmask_b32_e64 v9, v9, v12, s[12:13]
	v_mov_b32_e32 v11, vcc_hi
	v_mov_b32_e32 v12, vcc_lo
	v_cndmask_b32_e64 v9, v9, v11, s[14:15]
	v_cndmask_b32_e64 v2, v2, v12, s[14:15]
	v_cmp_ne_u32_e32 vcc, 0, v146
	s_nop 1
	v_mov_b32_e32 v10, vcc_lo
	v_mov_b32_e32 v11, vcc_hi
	v_cmp_ne_u32_e32 vcc, 0, v147
	v_cndmask_b32_e64 v2, v2, v10, s[16:17]
	v_cndmask_b32_e64 v8, v9, v11, s[16:17]
	v_mov_b32_e32 v9, vcc_hi
	v_mov_b32_e32 v10, vcc_lo
	v_cndmask_b32_e64 v9, v8, v9, s[18:19]
	v_cndmask_b32_e64 v8, v2, v10, s[18:19]
	s_mov_b64 s[2:3], exec
	s_mov_b64 exec, s[0:1]
	global_store_dwordx2 v[4:5], v[8:9], off
	s_mov_b64 exec, s[2:3]
	v_cmp_ne_u64_e32 vcc, 0, v[8:9]
	s_and_b64 s[20:21], s[0:1], vcc
	s_cmp_lg_u64 s[20:21], 0
	s_cselect_b32 s20, 32, 0
	s_or_b32 s76, s76, s20
	v_cmp_ne_u64_e32 vcc, -1, v[8:9]
	s_and_b64 s[20:21], s[0:1], vcc
	s_cmp_lg_u64 s[20:21], 0
	s_cselect_b32 s20, 32, 0
	s_or_b32 s77, s77, s20
	v_lshl_add_u64 v[4:5], v[4:5], 0, 8
	global_load_dword v196, v96, s[60:61] offset:3072 nt
	global_load_dword v197, v96, s[62:63] offset:3072 nt
	global_load_dword v198, v96, s[64:65] offset:3072 nt
	global_load_dword v199, v96, s[66:67] offset:3072 nt
	global_load_dword v200, v96, s[68:69] offset:3072 nt
	global_load_dword v201, v96, s[70:71] offset:3072 nt
	global_load_dword v202, v96, s[72:73] offset:3072 nt
	global_load_dword v203, v96, s[74:75] offset:3072 nt
	s_waitcnt vmcnt(54)
	v_cmp_ne_u32_e32 vcc, 0, v148
	s_nop 1
	v_mov_b32_e32 v2, vcc_lo
	v_mov_b32_e32 v9, vcc_hi
	v_cmp_ne_u32_e32 vcc, 0, v149
	v_cndmask_b32_e64 v2, 0, v2, s[22:23]
	v_cndmask_b32_e64 v9, 0, v9, s[22:23]
	v_mov_b32_e32 v11, vcc_hi
	v_mov_b32_e32 v14, vcc_lo
	v_cndmask_b32_e64 v9, v9, v11, s[6:7]
	v_cndmask_b32_e64 v2, v2, v14, s[6:7]
	v_cmp_ne_u32_e32 vcc, 0, v150
	s_nop 1
	v_mov_b32_e32 v11, vcc_lo
	v_mov_b32_e32 v14, vcc_hi
	v_cmp_ne_u32_e32 vcc, 0, v151
	v_cndmask_b32_e64 v2, v2, v11, s[8:9]
	v_cndmask_b32_e64 v9, v9, v14, s[8:9]
	v_mov_b32_e32 v11, vcc_hi
	v_mov_b32_e32 v14, vcc_lo
	v_cmp_ne_u32_e32 vcc, 0, v152
	v_cndmask_b32_e64 v9, v9, v11, s[10:11]
	v_cndmask_b32_e64 v2, v2, v14, s[10:11]
	v_mov_b32_e32 v11, vcc_lo
	v_mov_b32_e32 v12, vcc_hi
	v_cmp_ne_u32_e32 vcc, 0, v153
	v_cndmask_b32_e64 v2, v2, v11, s[12:13]
	v_cndmask_b32_e64 v9, v9, v12, s[12:13]
	v_mov_b32_e32 v11, vcc_hi
	v_mov_b32_e32 v12, vcc_lo
	v_cndmask_b32_e64 v9, v9, v11, s[14:15]
	v_cndmask_b32_e64 v2, v2, v12, s[14:15]
	v_cmp_ne_u32_e32 vcc, 0, v154
	s_nop 1
	v_mov_b32_e32 v10, vcc_lo
	v_mov_b32_e32 v11, vcc_hi
	v_cmp_ne_u32_e32 vcc, 0, v155
	v_cndmask_b32_e64 v2, v2, v10, s[16:17]
	v_cndmask_b32_e64 v8, v9, v11, s[16:17]
	v_mov_b32_e32 v9, vcc_hi
	v_mov_b32_e32 v10, vcc_lo
	v_cndmask_b32_e64 v9, v8, v9, s[18:19]
	v_cndmask_b32_e64 v8, v2, v10, s[18:19]
	s_mov_b64 s[2:3], exec
	s_mov_b64 exec, s[0:1]
	global_store_dwordx2 v[4:5], v[8:9], off
	s_mov_b64 exec, s[2:3]
	v_cmp_ne_u64_e32 vcc, 0, v[8:9]
	s_and_b64 s[20:21], s[0:1], vcc
	s_cmp_lg_u64 s[20:21], 0
	s_cselect_b32 s20, 64, 0
	s_or_b32 s76, s76, s20
	v_cmp_ne_u64_e32 vcc, -1, v[8:9]
	s_and_b64 s[20:21], s[0:1], vcc
	s_cmp_lg_u64 s[20:21], 0
	s_cselect_b32 s20, 64, 0
	s_or_b32 s77, s77, s20
	v_lshl_add_u64 v[4:5], v[4:5], 0, 8
	global_load_dword v204, v96, s[60:61] offset:3328 nt
	global_load_dword v205, v96, s[62:63] offset:3328 nt
	global_load_dword v206, v96, s[64:65] offset:3328 nt
	global_load_dword v207, v96, s[66:67] offset:3328 nt
	global_load_dword v208, v96, s[68:69] offset:3328 nt
	global_load_dword v209, v96, s[70:71] offset:3328 nt
	global_load_dword v210, v96, s[72:73] offset:3328 nt
	global_load_dword v211, v96, s[74:75] offset:3328 nt
	s_waitcnt vmcnt(54)
	v_cmp_ne_u32_e32 vcc, 0, v156
	s_nop 1
	v_mov_b32_e32 v2, vcc_lo
	v_mov_b32_e32 v9, vcc_hi
	v_cmp_ne_u32_e32 vcc, 0, v157
	v_cndmask_b32_e64 v2, 0, v2, s[22:23]
	v_cndmask_b32_e64 v9, 0, v9, s[22:23]
	v_mov_b32_e32 v11, vcc_hi
	v_mov_b32_e32 v14, vcc_lo
	v_cndmask_b32_e64 v9, v9, v11, s[6:7]
	v_cndmask_b32_e64 v2, v2, v14, s[6:7]
	v_cmp_ne_u32_e32 vcc, 0, v158
	s_nop 1
	v_mov_b32_e32 v11, vcc_lo
	v_mov_b32_e32 v14, vcc_hi
	v_cmp_ne_u32_e32 vcc, 0, v159
	v_cndmask_b32_e64 v2, v2, v11, s[8:9]
	v_cndmask_b32_e64 v9, v9, v14, s[8:9]
	v_mov_b32_e32 v11, vcc_hi
	v_mov_b32_e32 v14, vcc_lo
	v_cmp_ne_u32_e32 vcc, 0, v160
	v_cndmask_b32_e64 v9, v9, v11, s[10:11]
	v_cndmask_b32_e64 v2, v2, v14, s[10:11]
	v_mov_b32_e32 v11, vcc_lo
	v_mov_b32_e32 v12, vcc_hi
	v_cmp_ne_u32_e32 vcc, 0, v161
	v_cndmask_b32_e64 v2, v2, v11, s[12:13]
	v_cndmask_b32_e64 v9, v9, v12, s[12:13]
	v_mov_b32_e32 v11, vcc_hi
	v_mov_b32_e32 v12, vcc_lo
	v_cndmask_b32_e64 v9, v9, v11, s[14:15]
	v_cndmask_b32_e64 v2, v2, v12, s[14:15]
	v_cmp_ne_u32_e32 vcc, 0, v162
	s_nop 1
	v_mov_b32_e32 v10, vcc_lo
	v_mov_b32_e32 v11, vcc_hi
	v_cmp_ne_u32_e32 vcc, 0, v163
	v_cndmask_b32_e64 v2, v2, v10, s[16:17]
	v_cndmask_b32_e64 v8, v9, v11, s[16:17]
	v_mov_b32_e32 v9, vcc_hi
	v_mov_b32_e32 v10, vcc_lo
	v_cndmask_b32_e64 v9, v8, v9, s[18:19]
	v_cndmask_b32_e64 v8, v2, v10, s[18:19]
	s_mov_b64 s[2:3], exec
	s_mov_b64 exec, s[0:1]
	global_store_dwordx2 v[4:5], v[8:9], off
	s_mov_b64 exec, s[2:3]
	v_cmp_ne_u64_e32 vcc, 0, v[8:9]
	s_and_b64 s[20:21], s[0:1], vcc
	s_cmp_lg_u64 s[20:21], 0
	s_cselect_b32 s20, 128, 0
	s_or_b32 s76, s76, s20
	v_cmp_ne_u64_e32 vcc, -1, v[8:9]
	s_and_b64 s[20:21], s[0:1], vcc
	s_cmp_lg_u64 s[20:21], 0
	s_cselect_b32 s20, 128, 0
	s_or_b32 s77, s77, s20
	v_lshl_add_u64 v[4:5], v[4:5], 0, 8
	global_load_dword v212, v96, s[60:61] offset:3584 nt
	global_load_dword v213, v96, s[62:63] offset:3584 nt
	global_load_dword v214, v96, s[64:65] offset:3584 nt
	global_load_dword v215, v96, s[66:67] offset:3584 nt
	global_load_dword v216, v96, s[68:69] offset:3584 nt
	global_load_dword v217, v96, s[70:71] offset:3584 nt
	global_load_dword v218, v96, s[72:73] offset:3584 nt
	global_load_dword v219, v96, s[74:75] offset:3584 nt
	s_waitcnt vmcnt(54)
	v_cmp_ne_u32_e32 vcc, 0, v164
	s_nop 1
	v_mov_b32_e32 v2, vcc_lo
	v_mov_b32_e32 v9, vcc_hi
	v_cmp_ne_u32_e32 vcc, 0, v165
	v_cndmask_b32_e64 v2, 0, v2, s[22:23]
	v_cndmask_b32_e64 v9, 0, v9, s[22:23]
	v_mov_b32_e32 v11, vcc_hi
	v_mov_b32_e32 v14, vcc_lo
	v_cndmask_b32_e64 v9, v9, v11, s[6:7]
	v_cndmask_b32_e64 v2, v2, v14, s[6:7]
	v_cmp_ne_u32_e32 vcc, 0, v166
	s_nop 1
	v_mov_b32_e32 v11, vcc_lo
	v_mov_b32_e32 v14, vcc_hi
	v_cmp_ne_u32_e32 vcc, 0, v167
	v_cndmask_b32_e64 v2, v2, v11, s[8:9]
	v_cndmask_b32_e64 v9, v9, v14, s[8:9]
	v_mov_b32_e32 v11, vcc_hi
	v_mov_b32_e32 v14, vcc_lo
	v_cmp_ne_u32_e32 vcc, 0, v168
	v_cndmask_b32_e64 v9, v9, v11, s[10:11]
	v_cndmask_b32_e64 v2, v2, v14, s[10:11]
	v_mov_b32_e32 v11, vcc_lo
	v_mov_b32_e32 v12, vcc_hi
	v_cmp_ne_u32_e32 vcc, 0, v169
	v_cndmask_b32_e64 v2, v2, v11, s[12:13]
	v_cndmask_b32_e64 v9, v9, v12, s[12:13]
	v_mov_b32_e32 v11, vcc_hi
	v_mov_b32_e32 v12, vcc_lo
	v_cndmask_b32_e64 v9, v9, v11, s[14:15]
	v_cndmask_b32_e64 v2, v2, v12, s[14:15]
	v_cmp_ne_u32_e32 vcc, 0, v170
	s_nop 1
	v_mov_b32_e32 v10, vcc_lo
	v_mov_b32_e32 v11, vcc_hi
	v_cmp_ne_u32_e32 vcc, 0, v171
	v_cndmask_b32_e64 v2, v2, v10, s[16:17]
	v_cndmask_b32_e64 v8, v9, v11, s[16:17]
	v_mov_b32_e32 v9, vcc_hi
	v_mov_b32_e32 v10, vcc_lo
	v_cndmask_b32_e64 v9, v8, v9, s[18:19]
	v_cndmask_b32_e64 v8, v2, v10, s[18:19]
	s_mov_b64 s[2:3], exec
	s_mov_b64 exec, s[0:1]
	global_store_dwordx2 v[4:5], v[8:9], off
	s_mov_b64 exec, s[2:3]
	v_cmp_ne_u64_e32 vcc, 0, v[8:9]
	s_and_b64 s[20:21], s[0:1], vcc
	s_cmp_lg_u64 s[20:21], 0
	s_cselect_b32 s20, 256, 0
	s_or_b32 s76, s76, s20
	v_cmp_ne_u64_e32 vcc, -1, v[8:9]
	s_and_b64 s[20:21], s[0:1], vcc
	s_cmp_lg_u64 s[20:21], 0
	s_cselect_b32 s20, 256, 0
	s_or_b32 s77, s77, s20
	v_lshl_add_u64 v[4:5], v[4:5], 0, 8
	global_load_dword v220, v96, s[60:61] offset:3840 nt
	global_load_dword v221, v96, s[62:63] offset:3840 nt
	global_load_dword v222, v96, s[64:65] offset:3840 nt
	global_load_dword v223, v96, s[66:67] offset:3840 nt
	global_load_dword v224, v96, s[68:69] offset:3840 nt
	global_load_dword v225, v96, s[70:71] offset:3840 nt
	global_load_dword v226, v96, s[72:73] offset:3840 nt
	global_load_dword v227, v96, s[74:75] offset:3840 nt
	s_waitcnt vmcnt(54)
	v_cmp_ne_u32_e32 vcc, 0, v172
	s_nop 1
	v_mov_b32_e32 v2, vcc_lo
	v_mov_b32_e32 v9, vcc_hi
	v_cmp_ne_u32_e32 vcc, 0, v173
	v_cndmask_b32_e64 v2, 0, v2, s[22:23]
	v_cndmask_b32_e64 v9, 0, v9, s[22:23]
	v_mov_b32_e32 v11, vcc_hi
	v_mov_b32_e32 v14, vcc_lo
	v_cndmask_b32_e64 v9, v9, v11, s[6:7]
	v_cndmask_b32_e64 v2, v2, v14, s[6:7]
	v_cmp_ne_u32_e32 vcc, 0, v174
	s_nop 1
	v_mov_b32_e32 v11, vcc_lo
	v_mov_b32_e32 v14, vcc_hi
	v_cmp_ne_u32_e32 vcc, 0, v175
	v_cndmask_b32_e64 v2, v2, v11, s[8:9]
	v_cndmask_b32_e64 v9, v9, v14, s[8:9]
	v_mov_b32_e32 v11, vcc_hi
	v_mov_b32_e32 v14, vcc_lo
	v_cmp_ne_u32_e32 vcc, 0, v176
	v_cndmask_b32_e64 v9, v9, v11, s[10:11]
	v_cndmask_b32_e64 v2, v2, v14, s[10:11]
	v_mov_b32_e32 v11, vcc_lo
	v_mov_b32_e32 v12, vcc_hi
	v_cmp_ne_u32_e32 vcc, 0, v177
	v_cndmask_b32_e64 v2, v2, v11, s[12:13]
	v_cndmask_b32_e64 v9, v9, v12, s[12:13]
	v_mov_b32_e32 v11, vcc_hi
	v_mov_b32_e32 v12, vcc_lo
	v_cndmask_b32_e64 v9, v9, v11, s[14:15]
	v_cndmask_b32_e64 v2, v2, v12, s[14:15]
	v_cmp_ne_u32_e32 vcc, 0, v178
	s_nop 1
	v_mov_b32_e32 v10, vcc_lo
	v_mov_b32_e32 v11, vcc_hi
	v_cmp_ne_u32_e32 vcc, 0, v179
	v_cndmask_b32_e64 v2, v2, v10, s[16:17]
	v_cndmask_b32_e64 v8, v9, v11, s[16:17]
	v_mov_b32_e32 v9, vcc_hi
	v_mov_b32_e32 v10, vcc_lo
	v_cndmask_b32_e64 v9, v8, v9, s[18:19]
	v_cndmask_b32_e64 v8, v2, v10, s[18:19]
	s_mov_b64 s[2:3], exec
	s_mov_b64 exec, s[0:1]
	global_store_dwordx2 v[4:5], v[8:9], off
	s_mov_b64 exec, s[2:3]
	v_cmp_ne_u64_e32 vcc, 0, v[8:9]
	s_and_b64 s[20:21], s[0:1], vcc
	s_cmp_lg_u64 s[20:21], 0
	s_cselect_b32 s20, 512, 0
	s_or_b32 s76, s76, s20
	v_cmp_ne_u64_e32 vcc, -1, v[8:9]
	s_and_b64 s[20:21], s[0:1], vcc
	s_cmp_lg_u64 s[20:21], 0
	s_cselect_b32 s20, 512, 0
	s_or_b32 s77, s77, s20
	v_lshl_add_u64 v[4:5], v[4:5], 0, 8
	s_waitcnt vmcnt(46)
	v_cmp_ne_u32_e32 vcc, 0, v180
	s_nop 1
	v_mov_b32_e32 v2, vcc_lo
	v_mov_b32_e32 v9, vcc_hi
	v_cmp_ne_u32_e32 vcc, 0, v181
	v_cndmask_b32_e64 v2, 0, v2, s[22:23]
	v_cndmask_b32_e64 v9, 0, v9, s[22:23]
	v_mov_b32_e32 v11, vcc_hi
	v_mov_b32_e32 v14, vcc_lo
	v_cndmask_b32_e64 v9, v9, v11, s[6:7]
	v_cndmask_b32_e64 v2, v2, v14, s[6:7]
	v_cmp_ne_u32_e32 vcc, 0, v182
	s_nop 1
	v_mov_b32_e32 v11, vcc_lo
	v_mov_b32_e32 v14, vcc_hi
	v_cmp_ne_u32_e32 vcc, 0, v183
	v_cndmask_b32_e64 v2, v2, v11, s[8:9]
	v_cndmask_b32_e64 v9, v9, v14, s[8:9]
	v_mov_b32_e32 v11, vcc_hi
	v_mov_b32_e32 v14, vcc_lo
	v_cmp_ne_u32_e32 vcc, 0, v184
	v_cndmask_b32_e64 v9, v9, v11, s[10:11]
	v_cndmask_b32_e64 v2, v2, v14, s[10:11]
	v_mov_b32_e32 v11, vcc_lo
	v_mov_b32_e32 v12, vcc_hi
	v_cmp_ne_u32_e32 vcc, 0, v185
	v_cndmask_b32_e64 v2, v2, v11, s[12:13]
	v_cndmask_b32_e64 v9, v9, v12, s[12:13]
	v_mov_b32_e32 v11, vcc_hi
	v_mov_b32_e32 v12, vcc_lo
	v_cndmask_b32_e64 v9, v9, v11, s[14:15]
	v_cndmask_b32_e64 v2, v2, v12, s[14:15]
	v_cmp_ne_u32_e32 vcc, 0, v186
	s_nop 1
	v_mov_b32_e32 v10, vcc_lo
	v_mov_b32_e32 v11, vcc_hi
	v_cmp_ne_u32_e32 vcc, 0, v187
	v_cndmask_b32_e64 v2, v2, v10, s[16:17]
	v_cndmask_b32_e64 v8, v9, v11, s[16:17]
	v_mov_b32_e32 v9, vcc_hi
	v_mov_b32_e32 v10, vcc_lo
	v_cndmask_b32_e64 v9, v8, v9, s[18:19]
	v_cndmask_b32_e64 v8, v2, v10, s[18:19]
	s_mov_b64 s[2:3], exec
	s_mov_b64 exec, s[0:1]
	global_store_dwordx2 v[4:5], v[8:9], off
	s_mov_b64 exec, s[2:3]
	v_cmp_ne_u64_e32 vcc, 0, v[8:9]
	s_and_b64 s[20:21], s[0:1], vcc
	s_cmp_lg_u64 s[20:21], 0
	s_cselect_b32 s20, 1024, 0
	s_or_b32 s76, s76, s20
	v_cmp_ne_u64_e32 vcc, -1, v[8:9]
	s_and_b64 s[20:21], s[0:1], vcc
	s_cmp_lg_u64 s[20:21], 0
	s_cselect_b32 s20, 1024, 0
	s_or_b32 s77, s77, s20
	v_lshl_add_u64 v[4:5], v[4:5], 0, 8
	s_waitcnt vmcnt(38)
	v_cmp_ne_u32_e32 vcc, 0, v188
	s_nop 1
	v_mov_b32_e32 v2, vcc_lo
	v_mov_b32_e32 v9, vcc_hi
	v_cmp_ne_u32_e32 vcc, 0, v189
	v_cndmask_b32_e64 v2, 0, v2, s[22:23]
	v_cndmask_b32_e64 v9, 0, v9, s[22:23]
	v_mov_b32_e32 v11, vcc_hi
	v_mov_b32_e32 v14, vcc_lo
	v_cndmask_b32_e64 v9, v9, v11, s[6:7]
	v_cndmask_b32_e64 v2, v2, v14, s[6:7]
	v_cmp_ne_u32_e32 vcc, 0, v190
	s_nop 1
	v_mov_b32_e32 v11, vcc_lo
	v_mov_b32_e32 v14, vcc_hi
	v_cmp_ne_u32_e32 vcc, 0, v191
	v_cndmask_b32_e64 v2, v2, v11, s[8:9]
	v_cndmask_b32_e64 v9, v9, v14, s[8:9]
	v_mov_b32_e32 v11, vcc_hi
	v_mov_b32_e32 v14, vcc_lo
	v_cmp_ne_u32_e32 vcc, 0, v192
	v_cndmask_b32_e64 v9, v9, v11, s[10:11]
	v_cndmask_b32_e64 v2, v2, v14, s[10:11]
	v_mov_b32_e32 v11, vcc_lo
	v_mov_b32_e32 v12, vcc_hi
	v_cmp_ne_u32_e32 vcc, 0, v193
	v_cndmask_b32_e64 v2, v2, v11, s[12:13]
	v_cndmask_b32_e64 v9, v9, v12, s[12:13]
	v_mov_b32_e32 v11, vcc_hi
	v_mov_b32_e32 v12, vcc_lo
	v_cndmask_b32_e64 v9, v9, v11, s[14:15]
	v_cndmask_b32_e64 v2, v2, v12, s[14:15]
	v_cmp_ne_u32_e32 vcc, 0, v194
	s_nop 1
	v_mov_b32_e32 v10, vcc_lo
	v_mov_b32_e32 v11, vcc_hi
	v_cmp_ne_u32_e32 vcc, 0, v195
	v_cndmask_b32_e64 v2, v2, v10, s[16:17]
	v_cndmask_b32_e64 v8, v9, v11, s[16:17]
	v_mov_b32_e32 v9, vcc_hi
	v_mov_b32_e32 v10, vcc_lo
	v_cndmask_b32_e64 v9, v8, v9, s[18:19]
	v_cndmask_b32_e64 v8, v2, v10, s[18:19]
	s_mov_b64 s[2:3], exec
	s_mov_b64 exec, s[0:1]
	global_store_dwordx2 v[4:5], v[8:9], off
	s_mov_b64 exec, s[2:3]
	v_cmp_ne_u64_e32 vcc, 0, v[8:9]
	s_and_b64 s[20:21], s[0:1], vcc
	s_cmp_lg_u64 s[20:21], 0
	s_cselect_b32 s20, 2048, 0
	s_or_b32 s76, s76, s20
	v_cmp_ne_u64_e32 vcc, -1, v[8:9]
	s_and_b64 s[20:21], s[0:1], vcc
	s_cmp_lg_u64 s[20:21], 0
	s_cselect_b32 s20, 2048, 0
	s_or_b32 s77, s77, s20
	v_lshl_add_u64 v[4:5], v[4:5], 0, 8
	s_waitcnt vmcnt(30)
	v_cmp_ne_u32_e32 vcc, 0, v196
	s_nop 1
	v_mov_b32_e32 v2, vcc_lo
	v_mov_b32_e32 v9, vcc_hi
	v_cmp_ne_u32_e32 vcc, 0, v197
	v_cndmask_b32_e64 v2, 0, v2, s[22:23]
	v_cndmask_b32_e64 v9, 0, v9, s[22:23]
	v_mov_b32_e32 v11, vcc_hi
	v_mov_b32_e32 v14, vcc_lo
	v_cndmask_b32_e64 v9, v9, v11, s[6:7]
	v_cndmask_b32_e64 v2, v2, v14, s[6:7]
	v_cmp_ne_u32_e32 vcc, 0, v198
	s_nop 1
	v_mov_b32_e32 v11, vcc_lo
	v_mov_b32_e32 v14, vcc_hi
	v_cmp_ne_u32_e32 vcc, 0, v199
	v_cndmask_b32_e64 v2, v2, v11, s[8:9]
	v_cndmask_b32_e64 v9, v9, v14, s[8:9]
	v_mov_b32_e32 v11, vcc_hi
	v_mov_b32_e32 v14, vcc_lo
	v_cmp_ne_u32_e32 vcc, 0, v200
	v_cndmask_b32_e64 v9, v9, v11, s[10:11]
	v_cndmask_b32_e64 v2, v2, v14, s[10:11]
	v_mov_b32_e32 v11, vcc_lo
	v_mov_b32_e32 v12, vcc_hi
	v_cmp_ne_u32_e32 vcc, 0, v201
	v_cndmask_b32_e64 v2, v2, v11, s[12:13]
	v_cndmask_b32_e64 v9, v9, v12, s[12:13]
	v_mov_b32_e32 v11, vcc_hi
	v_mov_b32_e32 v12, vcc_lo
	v_cndmask_b32_e64 v9, v9, v11, s[14:15]
	v_cndmask_b32_e64 v2, v2, v12, s[14:15]
	v_cmp_ne_u32_e32 vcc, 0, v202
	s_nop 1
	v_mov_b32_e32 v10, vcc_lo
	v_mov_b32_e32 v11, vcc_hi
	v_cmp_ne_u32_e32 vcc, 0, v203
	v_cndmask_b32_e64 v2, v2, v10, s[16:17]
	v_cndmask_b32_e64 v8, v9, v11, s[16:17]
	v_mov_b32_e32 v9, vcc_hi
	v_mov_b32_e32 v10, vcc_lo
	v_cndmask_b32_e64 v9, v8, v9, s[18:19]
	v_cndmask_b32_e64 v8, v2, v10, s[18:19]
	s_mov_b64 s[2:3], exec
	s_mov_b64 exec, s[0:1]
	global_store_dwordx2 v[4:5], v[8:9], off
	s_mov_b64 exec, s[2:3]
	v_cmp_ne_u64_e32 vcc, 0, v[8:9]
	s_and_b64 s[20:21], s[0:1], vcc
	s_cmp_lg_u64 s[20:21], 0
	s_cselect_b32 s20, 4096, 0
	s_or_b32 s76, s76, s20
	v_cmp_ne_u64_e32 vcc, -1, v[8:9]
	s_and_b64 s[20:21], s[0:1], vcc
	s_cmp_lg_u64 s[20:21], 0
	s_cselect_b32 s20, 4096, 0
	s_or_b32 s77, s77, s20
	v_lshl_add_u64 v[4:5], v[4:5], 0, 8
	s_waitcnt vmcnt(22)
	v_cmp_ne_u32_e32 vcc, 0, v204
	s_nop 1
	v_mov_b32_e32 v2, vcc_lo
	v_mov_b32_e32 v9, vcc_hi
	v_cmp_ne_u32_e32 vcc, 0, v205
	v_cndmask_b32_e64 v2, 0, v2, s[22:23]
	v_cndmask_b32_e64 v9, 0, v9, s[22:23]
	v_mov_b32_e32 v11, vcc_hi
	v_mov_b32_e32 v14, vcc_lo
	v_cndmask_b32_e64 v9, v9, v11, s[6:7]
	v_cndmask_b32_e64 v2, v2, v14, s[6:7]
	v_cmp_ne_u32_e32 vcc, 0, v206
	s_nop 1
	v_mov_b32_e32 v11, vcc_lo
	v_mov_b32_e32 v14, vcc_hi
	v_cmp_ne_u32_e32 vcc, 0, v207
	v_cndmask_b32_e64 v2, v2, v11, s[8:9]
	v_cndmask_b32_e64 v9, v9, v14, s[8:9]
	v_mov_b32_e32 v11, vcc_hi
	v_mov_b32_e32 v14, vcc_lo
	v_cmp_ne_u32_e32 vcc, 0, v208
	v_cndmask_b32_e64 v9, v9, v11, s[10:11]
	v_cndmask_b32_e64 v2, v2, v14, s[10:11]
	v_mov_b32_e32 v11, vcc_lo
	v_mov_b32_e32 v12, vcc_hi
	v_cmp_ne_u32_e32 vcc, 0, v209
	v_cndmask_b32_e64 v2, v2, v11, s[12:13]
	v_cndmask_b32_e64 v9, v9, v12, s[12:13]
	v_mov_b32_e32 v11, vcc_hi
	v_mov_b32_e32 v12, vcc_lo
	v_cndmask_b32_e64 v9, v9, v11, s[14:15]
	v_cndmask_b32_e64 v2, v2, v12, s[14:15]
	v_cmp_ne_u32_e32 vcc, 0, v210
	s_nop 1
	v_mov_b32_e32 v10, vcc_lo
	v_mov_b32_e32 v11, vcc_hi
	v_cmp_ne_u32_e32 vcc, 0, v211
	v_cndmask_b32_e64 v2, v2, v10, s[16:17]
	v_cndmask_b32_e64 v8, v9, v11, s[16:17]
	v_mov_b32_e32 v9, vcc_hi
	v_mov_b32_e32 v10, vcc_lo
	v_cndmask_b32_e64 v9, v8, v9, s[18:19]
	v_cndmask_b32_e64 v8, v2, v10, s[18:19]
	s_mov_b64 s[2:3], exec
	s_mov_b64 exec, s[0:1]
	global_store_dwordx2 v[4:5], v[8:9], off
	s_mov_b64 exec, s[2:3]
	v_cmp_ne_u64_e32 vcc, 0, v[8:9]
	s_and_b64 s[20:21], s[0:1], vcc
	s_cmp_lg_u64 s[20:21], 0
	s_cselect_b32 s20, 8192, 0
	s_or_b32 s76, s76, s20
	v_cmp_ne_u64_e32 vcc, -1, v[8:9]
	s_and_b64 s[20:21], s[0:1], vcc
	s_cmp_lg_u64 s[20:21], 0
	s_cselect_b32 s20, 8192, 0
	s_or_b32 s77, s77, s20
	v_lshl_add_u64 v[4:5], v[4:5], 0, 8
	s_waitcnt vmcnt(14)
	v_cmp_ne_u32_e32 vcc, 0, v212
	s_nop 1
	v_mov_b32_e32 v2, vcc_lo
	v_mov_b32_e32 v9, vcc_hi
	v_cmp_ne_u32_e32 vcc, 0, v213
	v_cndmask_b32_e64 v2, 0, v2, s[22:23]
	v_cndmask_b32_e64 v9, 0, v9, s[22:23]
	v_mov_b32_e32 v11, vcc_hi
	v_mov_b32_e32 v14, vcc_lo
	v_cndmask_b32_e64 v9, v9, v11, s[6:7]
	v_cndmask_b32_e64 v2, v2, v14, s[6:7]
	v_cmp_ne_u32_e32 vcc, 0, v214
	s_nop 1
	v_mov_b32_e32 v11, vcc_lo
	v_mov_b32_e32 v14, vcc_hi
	v_cmp_ne_u32_e32 vcc, 0, v215
	v_cndmask_b32_e64 v2, v2, v11, s[8:9]
	v_cndmask_b32_e64 v9, v9, v14, s[8:9]
	v_mov_b32_e32 v11, vcc_hi
	v_mov_b32_e32 v14, vcc_lo
	v_cmp_ne_u32_e32 vcc, 0, v216
	v_cndmask_b32_e64 v9, v9, v11, s[10:11]
	v_cndmask_b32_e64 v2, v2, v14, s[10:11]
	v_mov_b32_e32 v11, vcc_lo
	v_mov_b32_e32 v12, vcc_hi
	v_cmp_ne_u32_e32 vcc, 0, v217
	v_cndmask_b32_e64 v2, v2, v11, s[12:13]
	v_cndmask_b32_e64 v9, v9, v12, s[12:13]
	v_mov_b32_e32 v11, vcc_hi
	v_mov_b32_e32 v12, vcc_lo
	v_cndmask_b32_e64 v9, v9, v11, s[14:15]
	v_cndmask_b32_e64 v2, v2, v12, s[14:15]
	v_cmp_ne_u32_e32 vcc, 0, v218
	s_nop 1
	v_mov_b32_e32 v10, vcc_lo
	v_mov_b32_e32 v11, vcc_hi
	v_cmp_ne_u32_e32 vcc, 0, v219
	v_cndmask_b32_e64 v2, v2, v10, s[16:17]
	v_cndmask_b32_e64 v8, v9, v11, s[16:17]
	v_mov_b32_e32 v9, vcc_hi
	v_mov_b32_e32 v10, vcc_lo
	v_cndmask_b32_e64 v9, v8, v9, s[18:19]
	v_cndmask_b32_e64 v8, v2, v10, s[18:19]
	s_mov_b64 s[2:3], exec
	s_mov_b64 exec, s[0:1]
	global_store_dwordx2 v[4:5], v[8:9], off
	s_mov_b64 exec, s[2:3]
	v_cmp_ne_u64_e32 vcc, 0, v[8:9]
	s_and_b64 s[20:21], s[0:1], vcc
	s_cmp_lg_u64 s[20:21], 0
	s_cselect_b32 s20, 16384, 0
	s_or_b32 s76, s76, s20
	v_cmp_ne_u64_e32 vcc, -1, v[8:9]
	s_and_b64 s[20:21], s[0:1], vcc
	s_cmp_lg_u64 s[20:21], 0
	s_cselect_b32 s20, 16384, 0
	s_or_b32 s77, s77, s20
	v_lshl_add_u64 v[4:5], v[4:5], 0, 8
	s_waitcnt vmcnt(6)
	v_cmp_ne_u32_e32 vcc, 0, v220
	s_nop 1
	v_mov_b32_e32 v2, vcc_lo
	v_mov_b32_e32 v9, vcc_hi
	v_cmp_ne_u32_e32 vcc, 0, v221
	v_cndmask_b32_e64 v2, 0, v2, s[22:23]
	v_cndmask_b32_e64 v9, 0, v9, s[22:23]
	v_mov_b32_e32 v11, vcc_hi
	v_mov_b32_e32 v14, vcc_lo
	v_cndmask_b32_e64 v9, v9, v11, s[6:7]
	v_cndmask_b32_e64 v2, v2, v14, s[6:7]
	v_cmp_ne_u32_e32 vcc, 0, v222
	s_nop 1
	v_mov_b32_e32 v11, vcc_lo
	v_mov_b32_e32 v14, vcc_hi
	v_cmp_ne_u32_e32 vcc, 0, v223
	v_cndmask_b32_e64 v2, v2, v11, s[8:9]
	v_cndmask_b32_e64 v9, v9, v14, s[8:9]
	v_mov_b32_e32 v11, vcc_hi
	v_mov_b32_e32 v14, vcc_lo
	v_cmp_ne_u32_e32 vcc, 0, v224
	v_cndmask_b32_e64 v9, v9, v11, s[10:11]
	v_cndmask_b32_e64 v2, v2, v14, s[10:11]
	v_mov_b32_e32 v11, vcc_lo
	v_mov_b32_e32 v12, vcc_hi
	v_cmp_ne_u32_e32 vcc, 0, v225
	v_cndmask_b32_e64 v2, v2, v11, s[12:13]
	v_cndmask_b32_e64 v9, v9, v12, s[12:13]
	v_mov_b32_e32 v11, vcc_hi
	v_mov_b32_e32 v12, vcc_lo
	v_cndmask_b32_e64 v9, v9, v11, s[14:15]
	v_cndmask_b32_e64 v2, v2, v12, s[14:15]
	v_cmp_ne_u32_e32 vcc, 0, v226
	s_nop 1
	v_mov_b32_e32 v10, vcc_lo
	v_mov_b32_e32 v11, vcc_hi
	v_cmp_ne_u32_e32 vcc, 0, v227
	v_cndmask_b32_e64 v2, v2, v10, s[16:17]
	v_cndmask_b32_e64 v8, v9, v11, s[16:17]
	v_mov_b32_e32 v9, vcc_hi
	v_mov_b32_e32 v10, vcc_lo
	v_cndmask_b32_e64 v9, v8, v9, s[18:19]
	v_cndmask_b32_e64 v8, v2, v10, s[18:19]
	s_mov_b64 s[2:3], exec
	s_mov_b64 exec, s[0:1]
	global_store_dwordx2 v[4:5], v[8:9], off
	s_mov_b64 exec, s[2:3]
	v_cmp_ne_u64_e32 vcc, 0, v[8:9]
	s_and_b64 s[20:21], s[0:1], vcc
	s_cmp_lg_u64 s[20:21], 0
	s_cselect_b32 s20, 32768, 0
	s_or_b32 s76, s76, s20
	v_cmp_ne_u64_e32 vcc, -1, v[8:9]
	s_and_b64 s[20:21], s[0:1], vcc
	s_cmp_lg_u64 s[20:21], 0
	s_cselect_b32 s20, 32768, 0
	s_or_b32 s77, s77, s20
	v_lshl_add_u64 v[4:5], v[4:5], 0, 8
	v_mov_b32_e32 v2, s76
	v_mov_b32_e32 v8, s77
	s_mov_b64 s[2:3], exec
	s_mov_b64 exec, s[22:23]
	ds_write2_b32 v1, v2, v8 offset1:8
	s_mov_b64 exec, s[2:3]
	s_waitcnt lgkmcnt(0)
	s_barrier
	ds_read_b128 v[8:11], v3
	ds_read_b128 v[12:15], v3 offset:16
	ds_read_b128 v[16:19], v3 offset:32
	ds_read_b128 v[20:23], v3 offset:48
	s_waitcnt lgkmcnt(0)
	v_or_b32_e32 v8, v8, v9
	v_or3_b32 v8, v8, v10, v11
	v_or3_b32 v8, v8, v12, v13
	v_or3_b32 v8, v8, v14, v15
	v_or_b32_e32 v16, v16, v17
	v_or3_b32 v16, v16, v18, v19
	v_or3_b32 v16, v16, v20, v21
	v_or3_b32 v16, v16, v22, v23
	v_and_b32_e32 v2, 15, v0
	v_lshrrev_b32_e32 v8, v2, v8
	v_and_b32_e32 v8, 1, v8
	v_lshrrev_b32_e32 v16, v2, v16
	v_and_b32_e32 v16, 1, v16
	v_lshl_or_b32 v8, v16, 1, v8
	v_lshlrev_b32_e32 v2, 2, v2
	v_cmp_gt_u32_e32 vcc, 16, v0
	s_and_saveexec_b64 s[2:3], vcc
	global_store_dword v2, v8, s[26:27]
	s_mov_b64 exec, s[2:3]
